# v18 + prologue de-serialisation (7.1): attention unit prologue QK(0) K-fragment reads issued up front with counted lgkmcnt waits (diff 8 reads, MLA 12 reads)
# baseline (speedup 1.0000x reference)
; #define LAS __attribute__((address_space(3)))
; __device__ __forceinline__ int v_rd_base(int lane) { return ((lane & 3) << 3) | (((lane >> 2) & 3) << 6) | (((lane >> 4) & 1) << 5) | (((lane >> 5) & 1) << 8); }
; #define DMA_WAIT(last) do { if (last) asm volatile("s_waitcnt vmcnt(0)" ::: "memory"); else asm volatile("s_waitcnt vmcnt(%0)" :: "n"(NPW) : "memory"); } while (0)
; template <int DK>
; __device__ __forceinline__ void qkt(f32x16& p0, f32x16& p1, const char* Ks, const bf16x8* qr, int r32, int hi) {
;   p0 = f32x16{}; p1 = f32x16{};
; #pragma unroll
;   for (int d0 = 0; d0 < DK / 16; ++d0) { const int cb = (d0 * 16 + hi * 8) * 2;
;     const bf16x8 b0 = *reinterpret_cast<const bf16x8*>(Ks + ATT_KSWZ(r32, cb));
;     const bf16x8 b1 = *reinterpret_cast<const bf16x8*>(Ks + ATT_KSWZ(32 + r32, cb));
;     p0 = __builtin_amdgcn_mfma_f32_32x32x16_bf16(b0, qr[d0], p0, 0, 0, 0);
;     p1 = __builtin_amdgcn_mfma_f32_32x32x16_bf16(b1, qr[d0], p1, 0, 0, 0);
;   }
; }
; template <int DK, int DV, bool OFF, class QLoader> ...
;     ...
;   QL.load(qr, wid * QBLK + r32, hi);
;   asm volatile("s_waitcnt vmcnt(0)" ::: "memory");
;   unsigned koff[KPW], voff[VPW];
; #pragma unroll
;   for (int i = 0; i < (DK == 64 ? 1 : KPW); ++i) { const int row = (wid * KPW + i) * 4 + (lane >> 4); int c = (lane & 15) ^ (row & 7); c = (c < DK / 8) ? c : (c & 7); koff[i] = (unsigned)((row * ldk) * 2 + c * 16); }
; #pragma unroll
;   for (int i = 0; i < 1; ++i) { const int sidx = (wid * VPW + i) * 2 + (lane >> 5), kg = sidx / ND, st = sidx % ND, kk = kg * 8 + ((lane & 31) >> 2);
;     const int k = (kk & ~0xC) | ((kk & 4) << 1) | ((kk & 8) >> 1), c = st * 32 + (lane & 3) * 8; voff[i] = (unsigned)((k * ldv + c) * 2); }
;   const int vb0 = (int)(uintptr_t)V_lds + v_rd_base(lane);
;   LAS unsigned* const ldsK = (LAS unsigned*)(LAS char*)K_lds + (wid * KPW) * 256; LAS unsigned* const ldsV = (LAS unsigned*)(LAS char*)V_lds + (wid * VPW) * 256;
;     ...
;   f32x16 pA0, pA1, pB0, pB1; bf16x8 pa0, pa1, pa2, pa3; const int NT = nkeys / KVBLK;
;   DMA_TILE(0, 0); DMA_TILE(1, 1); DMA_WAIT(false); __syncthreads(); if (2 < NT) DMA_TILE(2, 2);
;   qkt<DK>(pA0, pA1, K_lds, qr, r32, hi); partialSM<DK, OFF>(pA0, pA1, negMC);
.LBB0_838:
	s_and_b64 s[16:17], s[14:15], exec
	s_cselect_b32 s76, s12, s2
	s_ashr_i32 s2, s76, 4
	s_and_b32 s22, s76, 15
	s_mul_i32 s78, s76, 0x88000
	s_mul_hi_i32 s77, s76, 0x88000
	s_add_u32 s16, s65, s78
	s_addc_u32 s17, s66, s77
	s_lshl_b32 s4, s2, 8
	s_add_i32 s23, s4, 0x8000
	s_mul_i32 s80, s23, 0x1800
	s_mul_hi_i32 s79, s23, 0x1800
	s_add_u32 s4, s67, s80
	s_addc_u32 s12, s68, s79
	s_lshl_b32 s13, s76, 7
	s_and_b32 s13, s13, 0x700
	s_add_u32 s4, s4, s13
	s_addc_u32 s12, s12, 0
	s_add_u32 s18, s4, 0x1000
	s_addc_u32 s19, s12, 0
	s_lshl_b32 s12, s2, 12
	s_mul_i32 s2, s2, 0x1800000
	s_mul_hi_i32 s4, s12, 0x1800
	s_add_u32 s24, s67, s2
	s_addc_u32 s25, s68, s4
	s_add_u32 s13, s24, s13
	s_addc_u32 s24, s25, 0
	s_add_u32 s74, s13, 0x1000
	s_addc_u32 s75, s24, 0
	s_lshl_b32 s5, s5, 8
	s_or_b32 s5, s12, s5
	s_and_b64 s[12:13], s[14:15], exec
	s_cselect_b32 s12, s5, s23
	s_ashr_i32 s13, s12, 31
	s_lshl_b64 s[12:13], s[12:13], 12
	s_add_u32 s5, s69, s12
	s_addc_u32 s13, s70, s13
	s_lshl_b32 s12, s22, 8
	s_add_u32 s12, s5, s12
	s_addc_u32 s13, s13, 0
	s_andn2_b64 vcc, exec, s[34:35]
	s_mov_b64 s[22:23], -1
	s_cbranch_vccnz .LBB0_882
	v_mov_b32_e32 v25, v159
	v_mov_b32_e32 v33, v1
	v_readfirstlane_b32 s23, v25
	s_ashr_i32 s26, s23, 6
	v_and_b32_e32 v10, 31, v25
	s_lshl_b32 s22, s26, 5
	v_or_b32_e32 v2, s22, v10
	v_ashrrev_i32_e32 v3, 31, v2
	v_bfe_u32 v4, v25, 5, 1
	v_lshlrev_b64 v[2:3], 7, v[2:3]
	v_lshl_add_u64 v[2:3], s[20:21], 0, v[2:3]
	v_lshlrev_b32_e32 v32, 4, v4
	v_lshl_add_u64 v[2:3], v[2:3], 0, v[32:33]
	global_load_dwordx4 v[114:117], v[2:3], off
	global_load_dwordx4 v[118:121], v[2:3], off offset:32
	global_load_dwordx4 v[122:125], v[2:3], off offset:64
	global_load_dwordx4 v[126:129], v[2:3], off offset:96
	v_bfe_u32 v0, v25, 4, 2
	s_bfe_i32 s24, s26, 0x1001d
	v_and_b32_e32 v2, 15, v25
	v_bitop3_b32 v3, v0, v25, 15 bitop3:0x78
	v_lshl_or_b32 v20, s26, 2, v4
	s_lshr_b32 s24, s24, 30
	v_lshlrev_b32_e32 v3, 4, v3
	v_cmp_gt_u32_e32 vcc, 8, v2
	v_add_u32_e32 v2, s24, v20
	v_and_b32_e32 v5, 0x70, v3
	v_ashrrev_i32_e32 v21, 2, v2
	v_cndmask_b32_e32 v19, v5, v3, vcc
	v_lshlrev_b32_e32 v4, 3, v21
	v_bfe_u32 v5, v25, 2, 3
	v_bitop3_b32 v22, v4, -13, v5 bitop3:0xc8
	v_lshrrev_b32_e32 v4, 1, v25
	s_lshl_b32 s5, s26, 10
	v_lshlrev_b32_e32 v18, 7, v0
	v_and_b32_e32 v23, 8, v4
	v_and_b32_e32 v26, 4, v2
	v_or_b32_e32 v0, s5, v18
	v_and_b32_e32 v3, 0x3fffffc, v2
	v_or3_b32 v2, v23, v22, v26
	s_movk_i32 s24, 0xc00
	v_add_u32_e32 v0, v0, v19
	v_lshlrev_b32_e32 v4, 3, v25
	v_mul_lo_u32 v2, v2, s24
	s_add_i32 s27, 0, 0x10000
	s_lshl_b32 s24, s26, 11
	v_sub_u32_e32 v3, v20, v3
	v_and_b32_e32 v24, 24, v4
	s_add_i32 s81, s27, s5
	v_bfe_u32 v150, v25, 3, 3
	v_and_b32_e32 v0, 7, v25
	v_xor_b32_e32 v0, v0, v150
	v_lshlrev_b32_e32 v0, 4, v0
	v_lshl_or_b32 v0, v150, 7, v0
	v_or_b32_e32 v0, s5, v0
	v_mov_b32_e32 v151, v1
	v_lshl_or_b32 v3, v3, 5, v24
	s_add_i32 s82, s24, 0
	s_mov_b32 m0, s81
	v_lshl_add_u64 v[4:5], s[16:17], 0, v[150:151]
	s_mov_b64 s[24:25], 0x200
	s_add_i32 s83, s81, 0x400
	v_add_lshl_u32 v148, v3, v2, 1
	global_load_lds_dwordx4 v0, s[16:17]
	v_lshl_add_u64 v[6:7], v[4:5], 0, s[24:25]
	s_mov_b32 m0, s83
	v_mov_b32_e32 v149, v1
	v_lshl_add_u64 v[6:7], s[18:19], 0, v[148:149]
	s_mov_b32 m0, s82
	s_add_i32 s84, s82, 0x400
	v_lshl_add_u64 v[2:3], s[16:17], 0, v[0:1]
	global_load_lds_dwordx4 v148, s[18:19]
	v_lshl_add_u64 v[8:9], v[6:7], 0, s[10:11]
	s_mov_b32 m0, s84
	s_mov_b64 s[24:25], 0x2000
	s_add_i32 s85, s81, 0x4000
	global_load_lds_dwordx4 v[8:9], off
	v_lshl_add_u64 v[8:9], v[2:3], 0, s[24:25]
	s_mov_b32 m0, s85
	s_mov_b64 s[24:25], 0x2200
	s_add_i32 s86, s81, 0x4400
	global_load_lds_dwordx4 v[8:9], off
	v_lshl_add_u64 v[8:9], v[4:5], 0, s[24:25]
	s_mov_b32 m0, s86
	s_mov_b64 s[24:25], 0x60000
	s_add_i32 s87, s82, 0x4000
	v_lshl_add_u64 v[8:9], v[6:7], 0, s[24:25]
	s_mov_b32 m0, s87
	s_mov_b64 s[24:25], 0x60080
	s_add_i32 s88, s82, 0x4400
	global_load_lds_dwordx4 v[8:9], off
	v_lshl_add_u64 v[8:9], v[6:7], 0, s[24:25]
	s_mov_b32 m0, s88
	s_mov_b64 s[24:25], 0x4000
	s_add_i32 s89, s81, 0x8000
	global_load_lds_dwordx4 v[8:9], off
	v_lshl_add_u64 v[2:3], v[2:3], 0, s[24:25]
	s_mov_b32 m0, s89
	s_mov_b64 s[24:25], 0x4200
	s_add_i32 s90, s81, 0x8400
	s_waitcnt vmcnt(4)
	s_waitcnt vmcnt(0) lgkmcnt(0)
	s_barrier
	global_load_lds_dwordx4 v[2:3], off
	v_lshl_add_u64 v[2:3], v[4:5], 0, s[24:25]
	s_mov_b32 m0, s90
	s_mov_b64 s[24:25], 0xc0000
	s_add_i32 s91, s82, 0x8000
	v_lshl_add_u64 v[2:3], v[6:7], 0, s[24:25]
	s_mov_b32 m0, s91
	s_mov_b64 s[24:25], 0xc0080
	s_add_i32 s92, s82, 0x8400
	global_load_lds_dwordx4 v[2:3], off
	v_lshl_add_u64 v[2:3], v[6:7], 0, s[24:25]
	s_mov_b32 m0, s92
	v_lshlrev_b32_e32 v27, 7, v10
	global_load_lds_dwordx4 v[2:3], off
	v_lshlrev_b32_e32 v2, 4, v25
	v_and_b32_e32 v33, 0x70, v2
	v_bitop3_b32 v161, v32, v27, v33 bitop3:0xde
	v_add_u32_e32 v162, s27, v161
	v_or_b32_e32 v28, 32, v32
	v_bitop3_b32 v163, v28, v27, v33 bitop3:0xde
	v_add_u32_e32 v164, s27, v163
	v_or_b32_e32 v28, 64, v32
	v_bitop3_b32 v165, v28, v27, v33 bitop3:0xde
	v_add_u32_e32 v166, s27, v165
	v_or_b32_e32 v28, 0x60, v32
	v_bitop3_b32 v167, v28, v27, v33 bitop3:0xde
	v_add_u32_e32 v168, s27, v167
	ds_read_b128 v[216:219], v162
	ds_read_b128 v[220:223], v162 offset:4096
	ds_read_b128 v[224:227], v164
	ds_read_b128 v[228:231], v164 offset:4096
	ds_read_b128 v[232:235], v166
	ds_read_b128 v[236:239], v166 offset:4096
	ds_read_b128 v[240:243], v168
	ds_read_b128 v[244:247], v168 offset:4096
	s_cmp_lt_i32 s26, 4
	s_waitcnt lgkmcnt(6)
	v_mfma_f32_32x32x16_bf16 v[66:81], v[220:223], v[114:117], 0
	v_mfma_f32_32x32x16_bf16 v[2:17], v[216:219], v[114:117], 0
	s_waitcnt lgkmcnt(4)
	v_mfma_f32_32x32x16_bf16 v[2:17], v[224:227], v[118:121], v[2:17]
	v_mfma_f32_32x32x16_bf16 v[66:81], v[228:231], v[118:121], v[66:81]
	s_waitcnt lgkmcnt(2)
	v_mfma_f32_32x32x16_bf16 v[2:17], v[232:235], v[122:125], v[2:17]
	v_mfma_f32_32x32x16_bf16 v[66:81], v[236:239], v[122:125], v[66:81]
	s_waitcnt lgkmcnt(0)
	v_mfma_f32_32x32x16_bf16 v[2:17], v[240:243], v[126:129], v[2:17]
	v_mfma_f32_32x32x16_bf16 v[66:81], v[244:247], v[126:129], v[66:81]
	s_cbranch_scc1 .LBB0_841
	s_setprio 1

; #define LAS __attribute__((address_space(3)))
; template <int DK>
; __device__ __forceinline__ void qkt(f32x16& p0, f32x16& p1, const char* Ks, const bf16x8* qr, int r32, int hi) {
;   p0 = f32x16{}; p1 = f32x16{};
; #pragma unroll
;   for (int d0 = 0; d0 < DK / 16; ++d0) { const int cb = (d0 * 16 + hi * 8) * 2;
;     const bf16x8 b0 = *reinterpret_cast<const bf16x8*>(Ks + ATT_KSWZ(r32, cb));
;     const bf16x8 b1 = *reinterpret_cast<const bf16x8*>(Ks + ATT_KSWZ(32 + r32, cb));
;     p0 = __builtin_amdgcn_mfma_f32_32x32x16_bf16(b0, qr[d0], p0, 0, 0, 0);
;   __device__ __forceinline__ void load(bf16x8 (&qr)[6], int r, int hi) const {
;     ...
;     for (int d0 = 0; d0 < 6; ++d0) { const f32x4 g0 = *(const f32x4*)(gq + d0 * 16 + hi * 8), g1 = *(const f32x4*)(gq + d0 * 16 + hi * 8 + 4);
; #pragma unroll
;       for (int j = 0; j < 4; ++j) { v[d0][j] *= f * g0[j]; v[d0][4 + j] *= f * g1[j]; } }
;     if (cosA) { const float* c = cosA + (long)r * 16 + hi * 8; const float* sn = c + 4096 * 16;
; #pragma unroll
;       for (int j = 0; j < 8; ++j) { const float x1 = v[4][j], x2 = v[5][j], cs = c[j], si = sn[j]; v[4][j] = x1 * cs - x2 * si; v[5][j] = x1 * si + x2 * cs; } }
; #pragma unroll
;     for (int d0 = 0; d0 < 6; ++d0) qr[d0] = pack_bf8(v[d0]);
; template <int DK, int DV, bool OFF, class QLoader> ...
;     ...
;   unsigned koff[KPW], voff[VPW];
; #pragma unroll
;   for (int i = 0; i < (DK == 64 ? 1 : KPW); ++i) { const int row = (wid * KPW + i) * 4 + (lane >> 4); int c = (lane & 15) ^ (row & 7); c = (c < DK / 8) ? c : (c & 7); koff[i] = (unsigned)((row * ldk) * 2 + c * 16); }
; #pragma unroll
;   for (int i = 0; i < 1; ++i) { const int sidx = (wid * VPW + i) * 2 + (lane >> 5), kg = sidx / ND, st = sidx % ND, kk = kg * 8 + ((lane & 31) >> 2);
;     const int k = (kk & ~0xC) | ((kk & 4) << 1) | ((kk & 8) >> 1), c = st * 32 + (lane & 3) * 8; voff[i] = (unsigned)((k * ldv + c) * 2); }
;   const int vb0 = (int)(uintptr_t)V_lds + v_rd_base(lane);
;   LAS unsigned* const ldsK = (LAS unsigned*)(LAS char*)K_lds + (wid * KPW) * 256; LAS unsigned* const ldsV = (LAS unsigned*)(LAS char*)V_lds + (wid * VPW) * 256;
;     ...
;   f32x16 pA0, pA1, pB0, pB1; bf16x8 pa0, pa1, pa2, pa3; const int NT = nkeys / KVBLK;
;   DMA_TILE(0, 0); DMA_TILE(1, 1); DMA_WAIT(false); __syncthreads(); if (2 < NT) DMA_TILE(2, 2);
;   qkt<DK>(pA0, pA1, K_lds, qr, r32, hi); partialSM<DK, OFF>(pA0, pA1, negMC);
.LBB0_1415:
	v_and_b32_e32 v36, 63, v56
	v_mul_f32_e32 v0, v54, v33
	v_mul_f32_e32 v3, v3, v54
	v_mul_f32_e32 v0, v0, v88
	v_mul_f32_e32 v29, v54, v29
	v_mul_f32_e32 v32, v54, v32
	v_mul_f32_e32 v28, v54, v28
	v_mul_f32_e32 v31, v54, v31
	v_mul_f32_e32 v27, v54, v27
	v_mul_f32_e32 v30, v54, v30
	v_mul_f32_e32 v26, v54, v26
	v_mul_f32_e32 v25, v54, v25
	v_mul_f32_e32 v21, v21, v54
	v_mul_f32_e32 v24, v54, v24
	v_mul_f32_e32 v20, v20, v54
	v_mul_f32_e32 v23, v54, v23
	v_mul_f32_e32 v19, v19, v54
	v_mul_f32_e32 v22, v54, v22
	v_mul_f32_e32 v18, v18, v54
	v_mul_f32_e32 v17, v17, v54
	v_mul_f32_e32 v13, v13, v54
	v_mul_f32_e32 v16, v16, v54
	v_mul_f32_e32 v12, v12, v54
	v_mul_f32_e32 v15, v15, v54
	v_mul_f32_e32 v11, v11, v54
	v_mul_f32_e32 v14, v14, v54
	v_mul_f32_e32 v10, v10, v54
	v_mul_f32_e32 v9, v9, v54
	v_mul_f32_e32 v5, v5, v54
	v_mul_f32_e32 v8, v8, v54
	v_mul_f32_e32 v4, v4, v54
	v_mul_f32_e32 v7, v7, v54
	v_mul_f32_e32 v3, v3, v58
	v_mul_f32_e32 v6, v6, v54
	v_mul_f32_e32 v2, v2, v54
	v_lshrrev_b32_e32 v149, 4, v36
	v_mul_f32_e32 v29, v29, v86
	v_mul_f32_e32 v32, v32, v87
	v_mul_f32_e32 v28, v28, v84
	v_mul_f32_e32 v31, v31, v85
	v_mul_f32_e32 v27, v27, v82
	v_mul_f32_e32 v30, v30, v83
	v_mul_f32_e32 v26, v26, v81
	v_mul_f32_e32 v25, v25, v80
	v_mul_f32_e32 v21, v21, v78
	v_mul_f32_e32 v24, v24, v79
	v_mul_f32_e32 v20, v20, v76
	v_mul_f32_e32 v23, v23, v77
	v_mul_f32_e32 v19, v19, v74
	v_mul_f32_e32 v22, v22, v75
	v_mul_f32_e32 v18, v18, v73
	v_mul_f32_e32 v17, v17, v72
	v_mul_f32_e32 v13, v13, v70
	v_mul_f32_e32 v16, v16, v71
	v_mul_f32_e32 v12, v12, v68
	v_mul_f32_e32 v15, v15, v69
	v_mul_f32_e32 v11, v11, v66
	v_mul_f32_e32 v14, v14, v67
	v_mul_f32_e32 v10, v10, v65
	v_mul_f32_e32 v9, v9, v64
	v_mul_f32_e32 v5, v5, v62
	v_mul_f32_e32 v8, v8, v63
	v_mul_f32_e32 v4, v4, v60
	v_mul_f32_e32 v7, v7, v61
	v_mul_f32_e32 v6, v6, v59
	v_mul_f32_e32 v2, v2, v35
	v_cvt_pk_bf16_f32 v98, v2, v3
	v_cvt_pk_bf16_f32 v99, v4, v5
	v_cvt_pk_bf16_f32 v100, v6, v7
	v_cvt_pk_bf16_f32 v101, v8, v9
	v_cvt_pk_bf16_f32 v102, v10, v11
	v_cvt_pk_bf16_f32 v103, v12, v13
	v_cvt_pk_bf16_f32 v104, v14, v15
	v_cvt_pk_bf16_f32 v105, v16, v17
	v_cvt_pk_bf16_f32 v106, v18, v19
	v_cvt_pk_bf16_f32 v107, v20, v21
	v_cvt_pk_bf16_f32 v108, v22, v23
	v_cvt_pk_bf16_f32 v109, v24, v25
	v_cvt_pk_bf16_f32 v110, v26, v27
	v_cvt_pk_bf16_f32 v111, v28, v29
	v_cvt_pk_bf16_f32 v112, v30, v31
	v_cvt_pk_bf16_f32 v113, v32, v0
	v_lshl_or_b32 v0, s38, 3, v149
	v_bitop3_b32 v3, v149, v56, 15 bitop3:0x78
	s_movk_i32 s0, 0xc0
	v_and_b32_e32 v2, 15, v56
	v_mul_lo_u32 v4, v0, s0
	v_lshlrev_b32_e32 v0, 4, v3
	v_and_b32_e32 v3, 0x70, v0
	v_cmp_gt_u32_e32 vcc, 12, v2
	v_bitop3_b32 v2, v149, v2, 4 bitop3:0x36
	v_lshl_or_b32 v153, s38, 1, v57
	v_cndmask_b32_e32 v151, v3, v0, vcc
	v_lshlrev_b32_e32 v3, 4, v2
	v_cmp_gt_u32_e32 vcc, 12, v2
	v_lshrrev_b32_e32 v2, 31, v153
	v_and_b32_e32 v5, 0x70, v3
	v_add_u32_e32 v2, v153, v2
	v_cndmask_b32_e32 v150, v5, v3, vcc
	s_movk_i32 s0, 0x300
	v_ashrrev_i32_e32 v152, 1, v2
	v_add_u32_e32 v0, v151, v4
	v_add3_u32 v122, v4, v150, s0
	v_lshlrev_b32_e32 v3, 3, v152
	v_lshrrev_b32_e32 v4, 2, v55
	s_mov_b32 s0, 0x1fffff3
	v_bitop3_b32 v154, v3, s0, v4 bitop3:0xc8
	s_lshl_b32 s0, s38, 11
	v_lshrrev_b32_e32 v3, 1, v55
	s_add_i32 s87, s0, 0
	v_and_b32_e32 v2, 0x3fffffe, v2
	v_and_b32_e32 v155, 8, v3
	v_lshlrev_b32_e32 v3, 2, v152
	v_lshlrev_b32_e32 v4, 4, v56
	s_add_i32 s81, s87, 0x8000
	s_lshl_b32 s1, s38, 10
	v_cvt_pk_bf16_f32 v114, v50, v51
	v_cvt_pk_bf16_f32 v115, v52, v53
	v_cvt_pk_bf16_f32 v116, v40, v41
	v_cvt_pk_bf16_f32 v117, v46, v47
	v_cvt_pk_bf16_f32 v118, v44, v45
	v_cvt_pk_bf16_f32 v119, v48, v49
	v_cvt_pk_bf16_f32 v120, v38, v39
	v_cvt_pk_bf16_f32 v121, v42, v43
	s_waitcnt vmcnt(0)
	v_sub_u32_e32 v2, v153, v2
	v_and_b32_e32 v156, 4, v3
	v_and_b32_e32 v157, 48, v4
	s_sub_i32 s0, 0, s1
	s_sub_i32 s1, s87, s1
	s_mov_b32 m0, s81
	s_add_i32 s82, s87, 0x8400
	v_or3_b32 v3, v155, v154, v156
	v_lshl_or_b32 v2, v2, 6, v157
	s_mov_b32 m0, s82
	s_add_u32 s40, s20, 0x3000
	v_lshl_add_u32 v2, v3, 7, v2
	s_mov_b32 m0, s1
	s_addc_u32 s41, s21, 0
	s_add_i32 s83, s87, 0xc000
	s_mov_b32 m0, s83
	s_add_i32 s84, s87, 0xc400
	v_mov_b32_e32 v3, v1
	s_mov_b32 m0, s84
	v_lshl_add_u64 v[124:125], s[22:23], 0, v[2:3]
	s_mov_b64 s[40:41], 0x2000
	s_add_i32 m0, s1, 0x2000
	v_lshl_add_u64 v[2:3], v[124:125], 0, s[40:41]
	s_add_u32 s40, s20, 0x6000
	s_addc_u32 s41, s21, 0
	s_add_i32 m0, s87, 0x10000
	s_waitcnt vmcnt(3)
	s_waitcnt vmcnt(0) lgkmcnt(0)
	s_barrier
	global_load_lds_dwordx4 v0, s[40:41]
	s_add_i32 m0, s87, 0x10400
	v_lshlrev_b32_e32 v35, 8, v55
	global_load_lds_dwordx4 v122, s[40:41]
	s_mov_b64 s[40:41], 0x4000
	v_lshl_add_u64 v[2:3], v[124:125], 0, s[40:41]
	s_add_i32 m0, s1, 0x4000
	v_or_b32_e32 v38, 32, v34
	global_load_lds_dwordx4 v[2:3], off
	v_lshlrev_b32_e32 v2, 4, v55
	v_and_b32_e32 v37, 0x70, v2
	v_bitop3_b32 v140, v34, v35, v37 bitop3:0xde
	v_add_u32_e32 v126, 0, v140
	v_bitop3_b32 v141, v38, v35, v37 bitop3:0xde
	v_add_u32_e32 v127, 0, v141
	s_cmp_lt_i32 s38, 4
	v_or_b32_e32 v38, 64, v34
	v_bitop3_b32 v142, v38, v35, v37 bitop3:0xde
	v_add_u32_e32 v128, 0, v142
	v_or_b32_e32 v38, 0x60, v34
	v_bitop3_b32 v143, v38, v35, v37 bitop3:0xde
	v_add_u32_e32 v129, 0, v143
	v_or_b32_e32 v38, 0x80, v34
	v_bitop3_b32 v144, v38, v35, v37 bitop3:0xde
	v_add_u32_e32 v130, 0, v144
	v_or_b32_e32 v34, 0xa0, v34
	v_bitop3_b32 v145, v34, v35, v37 bitop3:0xde
	v_add_u32_e32 v131, 0, v145
	ds_read_b128 v[200:203], v126 offset:32768
	ds_read_b128 v[204:207], v126 offset:40960
	ds_read_b128 v[208:211], v127 offset:32768
	ds_read_b128 v[212:215], v127 offset:40960
	ds_read_b128 v[216:219], v128 offset:32768
	ds_read_b128 v[220:223], v128 offset:40960
	ds_read_b128 v[224:227], v129 offset:32768
	ds_read_b128 v[228:231], v129 offset:40960
	ds_read_b128 v[232:235], v130 offset:32768
	ds_read_b128 v[236:239], v130 offset:40960
	ds_read_b128 v[240:243], v131 offset:32768
	ds_read_b128 v[244:247], v131 offset:40960
	s_waitcnt lgkmcnt(10)
	v_mfma_f32_32x32x16_bf16 v[18:33], v[200:203], v[98:101], 0
	v_mfma_f32_32x32x16_bf16 v[2:17], v[204:207], v[98:101], 0
	s_waitcnt lgkmcnt(8)
	v_mfma_f32_32x32x16_bf16 v[18:33], v[208:211], v[102:105], v[18:33]
	v_mfma_f32_32x32x16_bf16 v[2:17], v[212:215], v[102:105], v[2:17]
	s_waitcnt lgkmcnt(6)
	v_mfma_f32_32x32x16_bf16 v[18:33], v[216:219], v[106:109], v[18:33]
	v_mfma_f32_32x32x16_bf16 v[2:17], v[220:223], v[106:109], v[2:17]
	s_waitcnt lgkmcnt(4)
	v_mfma_f32_32x32x16_bf16 v[18:33], v[224:227], v[110:113], v[18:33]
	v_mfma_f32_32x32x16_bf16 v[2:17], v[228:231], v[110:113], v[2:17]
	s_waitcnt lgkmcnt(2)
	v_mfma_f32_32x32x16_bf16 v[18:33], v[232:235], v[114:117], v[18:33]
	v_mfma_f32_32x32x16_bf16 v[2:17], v[236:239], v[114:117], v[2:17]
	s_waitcnt lgkmcnt(0)
	v_mfma_f32_32x32x16_bf16 v[18:33], v[240:243], v[118:121], v[18:33]
	v_mfma_f32_32x32x16_bf16 v[2:17], v[244:247], v[118:121], v[2:17]
	s_cbranch_scc1 .LBB0_1417
	s_setprio 1
